# v52: v51 K-frag hoist combined with merged ALiBi operand sdwa build (v49)
# baseline (speedup 1.0000x reference)
.Lw_win_4_done:
.LBB0_519:
	s_cmp_eq_u32 s32, 0
	s_cselect_b32 s84, 0, 1
	s_sub_u32 s32, s32, s84
	s_add_i32 s2, s29, s22
	s_add_i32 s3, s27, s21
	s_add_i32 s3, s3, -1
	s_and_b32 s31, s30, 0xc000
	s_add_i32 s33, s31, 0
	s_ashr_i32 s3, s3, 2
	s_add_i32 s31, s2, 0x7e0
	s_cmp_gt_i32 s31, s23
	v_cvt_f32_i32_e32 v111, s3
	s_cselect_b64 s[34:35], -1, 0
	s_add_i32 s3, s2, 0x7ff
	s_cmp_lt_i32 s3, s24
	s_cselect_b64 s[38:39], -1, 0
	v_add_u32_e32 v2, s33, v101
	v_add_u32_e32 v4, s33, v102
	v_add_u32_e32 v5, s33, v103
	v_add_u32_e32 v6, s33, v104
	s_or_b64 s[34:35], s[34:35], s[38:39]
	s_and_b64 vcc, exec, s[34:35]
	v_add_u32_e32 v115, v2, v100
	v_add_u32_e32 v114, v4, v100
	v_add_u32_e32 v113, v5, v100
	v_add_u32_e32 v112, v6, v100
	v_add_u32_e32 v16, s33, v105
	v_add_u32_e32 v17, s33, v106
	s_barrier
	s_cbranch_vccnz .Lkpre_skip_w
	ds_read_b128 v[4:7], v115 offset:4096
	ds_read_b128 v[188:191], v114 offset:4096
	ds_read_b128 v[192:195], v113 offset:4096
	ds_read_b128 v[202:205], v112 offset:4096
	s_and_b32 s31, s31, 0xe0
	v_or_b32_e32 v2, s31, v99
	v_cvt_f32_ubyte0_e32 v2, v2
	v_or_b32_sdwa v246, v2, v111 dst_sel:DWORD dst_unused:UNUSED_PAD src0_sel:DWORD src1_sel:WORD_1
	s_cmp_ge_i32 s20, s3
	s_cselect_b64 s[34:35], -1, 0
	s_waitcnt lgkmcnt(3)
	s_setprio 1
	v_mfma_f32_32x32x16_bf16 v[50:65], v[4:7], v[74:77], 0
	s_sub_i32 s3, s19, 32
	s_cmpk_lt_i32 s3, 0x1e1
	v_add3_u32 v116, v17, v94, s69
	s_cselect_b64 s[38:39], -1, 0
	s_and_b64 s[34:35], s[34:35], s[38:39]
	s_and_b64 vcc, exec, s[34:35]
	s_waitcnt lgkmcnt(2)
	v_mfma_f32_32x32x16_bf16 v[50:65], v[188:191], v[66:69], v[50:65]
	s_waitcnt lgkmcnt(1)
	v_mfma_f32_32x32x16_bf16 v[50:65], v[192:195], v[70:73], v[50:65]
	s_waitcnt lgkmcnt(0)
	v_mfma_f32_32x32x16_bf16 v[50:65], v[202:205], v[78:81], v[50:65]
	v_mfma_f32_32x32x16_bf16 v[50:65], v[246:249], v[82:85], v[50:65]
	v_add3_u32 v2, v16, v94, s69
	ds_read_b64_tr_b16 v[86:87], v2
	ds_read_b64_tr_b16 v[88:89], v2 offset:1024
	ds_read_b64_tr_b16 v[12:13], v116
	ds_read_b64_tr_b16 v[14:15], v116 offset:1024
	ds_read_b64_tr_b16 v[8:9], v2 offset:2048
	ds_read_b64_tr_b16 v[10:11], v2 offset:3072
	ds_read_b64_tr_b16 v[4:5], v116 offset:2048
	ds_read_b64_tr_b16 v[6:7], v116 offset:3072
	ds_read_b128 v[188:191], v115
	ds_read_b128 v[192:195], v114
	ds_read_b128 v[202:205], v113
	s_cbranch_vccnz .LBB0_524
	v_add_u32_e32 v2, s19, v108
	v_subrev_u32_e32 v116, 32, v2
	v_cmp_gt_u32_e32 vcc, s79, v116
	v_add3_u32 v116, v109, s22, 32
	s_nop 5
	v_cndmask_b32_e32 v50, v197, v50, vcc
	v_cmp_lt_u32_e32 vcc, s80, v116
	v_subrev_u32_e32 v116, 34, v2
	s_nop 0
	v_cndmask_b32_e32 v51, v197, v51, vcc
	v_cmp_gt_u32_e32 vcc, s79, v116
	v_subrev_u32_e32 v116, 35, v2
	s_nop 0
	v_cndmask_b32_e32 v52, v197, v52, vcc
	v_cmp_gt_u32_e32 vcc, s79, v116
	v_subrev_u32_e32 v116, 40, v2
	s_nop 0
	v_cndmask_b32_e32 v53, v197, v53, vcc
	v_cmp_gt_u32_e32 vcc, s79, v116
	v_subrev_u32_e32 v116, 41, v2
	s_nop 0
	v_cndmask_b32_e32 v54, v197, v54, vcc
	v_cmp_gt_u32_e32 vcc, s79, v116
	v_subrev_u32_e32 v116, 42, v2
	s_nop 0
	v_cndmask_b32_e32 v55, v197, v55, vcc
	v_cmp_gt_u32_e32 vcc, s79, v116
	v_subrev_u32_e32 v116, 43, v2
	s_nop 0
	v_cndmask_b32_e32 v56, v197, v56, vcc
	v_cmp_gt_u32_e32 vcc, s79, v116
	v_subrev_u32_e32 v116, 48, v2
	s_nop 0
	v_cndmask_b32_e32 v57, v197, v57, vcc
	v_cmp_gt_u32_e32 vcc, s79, v116
	v_subrev_u32_e32 v116, 49, v2
	s_nop 0
	v_cndmask_b32_e32 v58, v197, v58, vcc
	v_cmp_gt_u32_e32 vcc, s79, v116
	v_subrev_u32_e32 v116, 50, v2
	s_nop 0
	v_cndmask_b32_e32 v59, v197, v59, vcc
	v_cmp_gt_u32_e32 vcc, s79, v116
	v_subrev_u32_e32 v116, 51, v2
	s_nop 0
	v_cndmask_b32_e32 v60, v197, v60, vcc
	v_cmp_gt_u32_e32 vcc, s79, v116
	v_subrev_u32_e32 v116, 56, v2
	s_nop 0
	v_cndmask_b32_e32 v61, v197, v61, vcc
	v_cmp_gt_u32_e32 vcc, s79, v116
	v_subrev_u32_e32 v116, 57, v2
	s_nop 0
	v_cndmask_b32_e32 v62, v197, v62, vcc
	v_cmp_gt_u32_e32 vcc, s79, v116
	v_subrev_u32_e32 v116, 58, v2
	v_subrev_u32_e32 v2, 59, v2
	v_cndmask_b32_e32 v63, v197, v63, vcc
	v_cmp_gt_u32_e32 vcc, s79, v116
	s_nop 1
	v_cndmask_b32_e32 v64, v197, v64, vcc
	v_cmp_gt_u32_e32 vcc, s79, v2
	s_nop 1
	v_cndmask_b32_e32 v65, v197, v65, vcc

.Lring_issue_skip_0:
	s_add_i32 s3, s2, 0x7c0
	s_cmp_gt_i32 s3, s23
	s_cselect_b64 s[34:35], -1, 0
	s_addk_i32 s2, 0x7df
	s_cmp_lt_i32 s2, s24
	s_cselect_b64 s[38:39], -1, 0
	s_or_b64 s[34:35], s[34:35], s[38:39]
	s_and_b64 vcc, exec, s[34:35]
	s_cbranch_vccnz .LBB0_510
	ds_read_b128 v[4:7], v112
	s_and_b32 s3, s3, 0xc0
	v_or_b32_e32 v2, s3, v99
	v_cvt_f32_ubyte0_e32 v2, v2
	v_or_b32_sdwa v246, v2, v111 dst_sel:DWORD dst_unused:UNUSED_PAD src0_sel:DWORD src1_sel:WORD_1
	s_cmp_ge_i32 s20, s2
	s_cselect_b64 s[2:3], -1, 0
	s_waitcnt lgkmcnt(1)
	s_setprio 1
	v_mfma_f32_32x32x16_bf16 v[50:65], v[188:191], v[74:77], 0
	s_cmpk_lt_i32 s19, 0x1e1
	s_cselect_b64 s[34:35], -1, 0
	s_and_b64 s[2:3], s[2:3], s[34:35]
	s_and_b64 vcc, exec, s[2:3]
	v_mfma_f32_32x32x16_bf16 v[50:65], v[192:195], v[66:69], v[50:65]
	v_mfma_f32_32x32x16_bf16 v[50:65], v[202:205], v[70:73], v[50:65]
	s_waitcnt lgkmcnt(0)
	v_mfma_f32_32x32x16_bf16 v[50:65], v[4:7], v[78:81], v[50:65]
	v_mfma_f32_32x32x16_bf16 v[50:65], v[246:249], v[82:85], v[50:65]
	v_add3_u32 v2, v16, v94, s67
	v_add3_u32 v16, v17, v94, s67
	ds_read_b64_tr_b16 v[86:87], v2
	ds_read_b64_tr_b16 v[88:89], v2 offset:1024
	ds_read_b64_tr_b16 v[12:13], v16
	ds_read_b64_tr_b16 v[14:15], v16 offset:1024
	ds_read_b64_tr_b16 v[8:9], v2 offset:2048
	ds_read_b64_tr_b16 v[10:11], v2 offset:3072
	ds_read_b64_tr_b16 v[4:5], v16 offset:2048
	ds_read_b64_tr_b16 v[6:7], v16 offset:3072
	s_cbranch_vccnz .LBB0_530
	v_add_u32_e32 v2, s19, v108
	v_cmp_gt_u32_e32 vcc, s79, v2
	v_add_u32_e32 v16, s22, v109
	s_nop 5
	v_cndmask_b32_e32 v50, v197, v50, vcc
	v_cmp_lt_u32_e32 vcc, s80, v16
	v_add_u32_e32 v16, -2, v2
	s_nop 0
	v_cndmask_b32_e32 v51, v197, v51, vcc
	v_cmp_gt_u32_e32 vcc, s79, v16
	v_add_u32_e32 v16, -3, v2
	s_nop 0
	v_cndmask_b32_e32 v52, v197, v52, vcc
	v_cmp_gt_u32_e32 vcc, s79, v16
	v_add_u32_e32 v16, -8, v2
	s_nop 0
	v_cndmask_b32_e32 v53, v197, v53, vcc
	v_cmp_gt_u32_e32 vcc, s79, v16
	v_add_u32_e32 v16, -9, v2
	s_nop 0
	v_cndmask_b32_e32 v54, v197, v54, vcc
	v_cmp_gt_u32_e32 vcc, s79, v16
	v_add_u32_e32 v16, -10, v2
	s_nop 0
	v_cndmask_b32_e32 v55, v197, v55, vcc
	v_cmp_gt_u32_e32 vcc, s79, v16
	v_add_u32_e32 v16, -11, v2
	s_nop 0
	v_cndmask_b32_e32 v56, v197, v56, vcc
	v_cmp_gt_u32_e32 vcc, s79, v16
	v_add_u32_e32 v16, -16, v2
	s_nop 0
	v_cndmask_b32_e32 v57, v197, v57, vcc
	v_cmp_gt_u32_e32 vcc, s79, v16
	v_subrev_u32_e32 v16, 17, v2
	s_nop 0
	v_cndmask_b32_e32 v58, v197, v58, vcc
	v_cmp_gt_u32_e32 vcc, s79, v16
	v_subrev_u32_e32 v16, 18, v2
	s_nop 0
	v_cndmask_b32_e32 v59, v197, v59, vcc
	v_cmp_gt_u32_e32 vcc, s79, v16
	v_subrev_u32_e32 v16, 19, v2
	s_nop 0
	v_cndmask_b32_e32 v60, v197, v60, vcc
	v_cmp_gt_u32_e32 vcc, s79, v16
	v_subrev_u32_e32 v16, 24, v2
	s_nop 0
	v_cndmask_b32_e32 v61, v197, v61, vcc
	v_cmp_gt_u32_e32 vcc, s79, v16
	v_subrev_u32_e32 v16, 25, v2
	s_nop 0
	v_cndmask_b32_e32 v62, v197, v62, vcc
	v_cmp_gt_u32_e32 vcc, s79, v16
	v_subrev_u32_e32 v16, 26, v2
	v_subrev_u32_e32 v2, 27, v2
	v_cndmask_b32_e32 v63, v197, v63, vcc
	v_cmp_gt_u32_e32 vcc, s79, v16
	s_nop 1
	v_cndmask_b32_e32 v64, v197, v64, vcc
	v_cmp_gt_u32_e32 vcc, s79, v2
	s_nop 1
	v_cndmask_b32_e32 v65, v197, v65, vcc

.Lw_swa_4_done:
.LBB0_780:
	s_cmp_eq_u32 s32, 0
	s_cselect_b32 s84, 0, 1
	s_sub_u32 s32, s32, s84
	s_add_i32 s0, s25, s17
	s_add_i32 s1, s23, s18
	s_add_i32 s1, s1, -1
	s_and_b32 s27, s26, 0xc000
	s_add_i32 s34, s27, 0
	s_ashr_i32 s1, s1, 2
	s_add_i32 s27, s0, 0x7e0
	s_cmp_gt_i32 s27, s19
	v_cvt_f32_i32_e32 v114, s1
	s_cselect_b64 s[28:29], -1, 0
	s_add_i32 s1, s0, 0x7ff
	s_cmp_lt_i32 s1, s20
	s_cselect_b64 s[30:31], -1, 0
	v_add_u32_e32 v2, s34, v104
	v_add_u32_e32 v4, s34, v105
	v_add_u32_e32 v5, s34, v106
	v_add_u32_e32 v6, s34, v107
	s_or_b64 s[28:29], s[28:29], s[30:31]
	s_and_b64 vcc, exec, s[28:29]
	v_add_u32_e32 v118, v2, v103
	v_add_u32_e32 v117, v4, v103
	v_add_u32_e32 v116, v5, v103
	v_add_u32_e32 v115, v6, v103
	v_add_u32_e32 v16, s34, v109
	v_add_u32_e32 v17, s34, v110
	s_barrier
	s_cbranch_vccnz .Lkpre_skip_s
	ds_read_b128 v[4:7], v118 offset:4096
	ds_read_b128 v[188:191], v117 offset:4096
	ds_read_b128 v[192:195], v116 offset:4096
	ds_read_b128 v[202:205], v115 offset:4096
	s_and_b32 s27, s27, 0xe0
	v_or_b32_e32 v2, s27, v102
	v_cvt_f32_ubyte0_e32 v2, v2
	v_or_b32_sdwa v246, v2, v114 dst_sel:DWORD dst_unused:UNUSED_PAD src0_sel:DWORD src1_sel:WORD_1
	s_cmp_ge_i32 s16, s1
	s_cselect_b64 s[28:29], -1, 0
	s_waitcnt lgkmcnt(3)
	s_setprio 1
	v_mfma_f32_32x32x16_bf16 v[50:65], v[4:7], v[66:69], 0
	s_sub_i32 s1, s15, 32
	s_cmpk_lt_i32 s1, 0x61
	v_add3_u32 v119, v17, v96, s69
	s_cselect_b64 s[30:31], -1, 0
	s_and_b64 s[28:29], s[28:29], s[30:31]
	s_and_b64 vcc, exec, s[28:29]
	s_waitcnt lgkmcnt(2)
	v_mfma_f32_32x32x16_bf16 v[50:65], v[188:191], v[70:73], v[50:65]
	s_waitcnt lgkmcnt(1)
	v_mfma_f32_32x32x16_bf16 v[50:65], v[192:195], v[74:77], v[50:65]
	s_waitcnt lgkmcnt(0)
	v_mfma_f32_32x32x16_bf16 v[50:65], v[202:205], v[78:81], v[50:65]
	v_mfma_f32_32x32x16_bf16 v[50:65], v[246:249], v[82:85], v[50:65]
	v_add3_u32 v2, v16, v96, s69
	ds_read_b64_tr_b16 v[86:87], v2
	ds_read_b64_tr_b16 v[88:89], v2 offset:1024
	ds_read_b64_tr_b16 v[12:13], v119
	ds_read_b64_tr_b16 v[14:15], v119 offset:1024
	ds_read_b64_tr_b16 v[8:9], v2 offset:2048
	ds_read_b64_tr_b16 v[10:11], v2 offset:3072
	ds_read_b64_tr_b16 v[4:5], v119 offset:2048
	ds_read_b64_tr_b16 v[6:7], v119 offset:3072
	ds_read_b128 v[188:191], v118
	ds_read_b128 v[192:195], v117
	ds_read_b128 v[202:205], v116
	s_cbranch_vccnz .LBB0_785
	v_add_u32_e32 v2, s15, v111
	v_subrev_u32_e32 v119, 32, v2
	v_cmp_gt_u32_e32 vcc, s71, v119
	v_add3_u32 v119, v112, s17, 32
	s_nop 5
	v_cndmask_b32_e32 v50, v197, v50, vcc
	v_cmp_lt_u32_e32 vcc, s47, v119
	v_subrev_u32_e32 v119, 34, v2
	s_nop 0
	v_cndmask_b32_e32 v51, v197, v51, vcc
	v_cmp_gt_u32_e32 vcc, s71, v119
	v_subrev_u32_e32 v119, 35, v2
	s_nop 0
	v_cndmask_b32_e32 v52, v197, v52, vcc
	v_cmp_gt_u32_e32 vcc, s71, v119
	v_subrev_u32_e32 v119, 40, v2
	s_nop 0
	v_cndmask_b32_e32 v53, v197, v53, vcc
	v_cmp_gt_u32_e32 vcc, s71, v119
	v_subrev_u32_e32 v119, 41, v2
	s_nop 0
	v_cndmask_b32_e32 v54, v197, v54, vcc
	v_cmp_gt_u32_e32 vcc, s71, v119
	v_subrev_u32_e32 v119, 42, v2
	s_nop 0
	v_cndmask_b32_e32 v55, v197, v55, vcc
	v_cmp_gt_u32_e32 vcc, s71, v119
	v_subrev_u32_e32 v119, 43, v2
	s_nop 0
	v_cndmask_b32_e32 v56, v197, v56, vcc
	v_cmp_gt_u32_e32 vcc, s71, v119
	v_subrev_u32_e32 v119, 48, v2
	s_nop 0
	v_cndmask_b32_e32 v57, v197, v57, vcc
	v_cmp_gt_u32_e32 vcc, s71, v119
	v_subrev_u32_e32 v119, 49, v2
	s_nop 0
	v_cndmask_b32_e32 v58, v197, v58, vcc
	v_cmp_gt_u32_e32 vcc, s71, v119
	v_subrev_u32_e32 v119, 50, v2
	s_nop 0
	v_cndmask_b32_e32 v59, v197, v59, vcc
	v_cmp_gt_u32_e32 vcc, s71, v119
	v_subrev_u32_e32 v119, 51, v2
	s_nop 0
	v_cndmask_b32_e32 v60, v197, v60, vcc
	v_cmp_gt_u32_e32 vcc, s71, v119
	v_subrev_u32_e32 v119, 56, v2
	s_nop 0
	v_cndmask_b32_e32 v61, v197, v61, vcc
	v_cmp_gt_u32_e32 vcc, s71, v119
	v_subrev_u32_e32 v119, 57, v2
	s_nop 0
	v_cndmask_b32_e32 v62, v197, v62, vcc
	v_cmp_gt_u32_e32 vcc, s71, v119
	v_subrev_u32_e32 v119, 58, v2
	v_subrev_u32_e32 v2, 59, v2
	v_cndmask_b32_e32 v63, v197, v63, vcc
	v_cmp_gt_u32_e32 vcc, s71, v119
	s_nop 1
	v_cndmask_b32_e32 v64, v197, v64, vcc
	v_cmp_gt_u32_e32 vcc, s71, v2
	s_nop 1
	v_cndmask_b32_e32 v65, v197, v65, vcc

.Lring_issue_skip_1:
	s_add_i32 s1, s0, 0x7c0
	s_cmp_gt_i32 s1, s19
	s_cselect_b64 s[28:29], -1, 0
	s_addk_i32 s0, 0x7df
	s_cmp_lt_i32 s0, s20
	s_cselect_b64 s[30:31], -1, 0
	s_or_b64 s[28:29], s[28:29], s[30:31]
	s_and_b64 vcc, exec, s[28:29]
	s_cbranch_vccnz .LBB0_771
	ds_read_b128 v[4:7], v115
	s_and_b32 s1, s1, 0xc0
	v_or_b32_e32 v2, s1, v102
	v_cvt_f32_ubyte0_e32 v2, v2
	v_or_b32_sdwa v246, v2, v114 dst_sel:DWORD dst_unused:UNUSED_PAD src0_sel:DWORD src1_sel:WORD_1
	s_cmp_ge_i32 s16, s0
	s_cselect_b64 s[0:1], -1, 0
	s_waitcnt lgkmcnt(1)
	s_setprio 1
	v_mfma_f32_32x32x16_bf16 v[50:65], v[188:191], v[66:69], 0
	s_cmpk_lt_i32 s15, 0x61
	s_cselect_b64 s[28:29], -1, 0
	s_and_b64 s[0:1], s[0:1], s[28:29]
	s_and_b64 vcc, exec, s[0:1]
	v_mfma_f32_32x32x16_bf16 v[50:65], v[192:195], v[70:73], v[50:65]
	v_mfma_f32_32x32x16_bf16 v[50:65], v[202:205], v[74:77], v[50:65]
	s_waitcnt lgkmcnt(0)
	v_mfma_f32_32x32x16_bf16 v[50:65], v[4:7], v[78:81], v[50:65]
	v_mfma_f32_32x32x16_bf16 v[50:65], v[246:249], v[82:85], v[50:65]
	v_add3_u32 v2, v16, v96, s67
	v_add3_u32 v16, v17, v96, s67
	ds_read_b64_tr_b16 v[86:87], v2
	ds_read_b64_tr_b16 v[88:89], v2 offset:1024
	ds_read_b64_tr_b16 v[12:13], v16
	ds_read_b64_tr_b16 v[14:15], v16 offset:1024
	ds_read_b64_tr_b16 v[8:9], v2 offset:2048
	ds_read_b64_tr_b16 v[10:11], v2 offset:3072
	ds_read_b64_tr_b16 v[4:5], v16 offset:2048
	ds_read_b64_tr_b16 v[6:7], v16 offset:3072
	s_cbranch_vccnz .LBB0_791
	v_add_u32_e32 v2, s15, v111
	v_cmp_gt_u32_e32 vcc, s71, v2
	v_add_u32_e32 v16, s17, v112
	s_nop 5
	v_cndmask_b32_e32 v50, v197, v50, vcc
	v_cmp_lt_u32_e32 vcc, s47, v16
	v_add_u32_e32 v16, -2, v2
	s_nop 0
	v_cndmask_b32_e32 v51, v197, v51, vcc
	v_cmp_gt_u32_e32 vcc, s71, v16
	v_add_u32_e32 v16, -3, v2
	s_nop 0
	v_cndmask_b32_e32 v52, v197, v52, vcc
	v_cmp_gt_u32_e32 vcc, s71, v16
	v_add_u32_e32 v16, -8, v2
	s_nop 0
	v_cndmask_b32_e32 v53, v197, v53, vcc
	v_cmp_gt_u32_e32 vcc, s71, v16
	v_add_u32_e32 v16, -9, v2
	s_nop 0
	v_cndmask_b32_e32 v54, v197, v54, vcc
	v_cmp_gt_u32_e32 vcc, s71, v16
	v_add_u32_e32 v16, -10, v2
	s_nop 0
	v_cndmask_b32_e32 v55, v197, v55, vcc
	v_cmp_gt_u32_e32 vcc, s71, v16
	v_add_u32_e32 v16, -11, v2
	s_nop 0
	v_cndmask_b32_e32 v56, v197, v56, vcc
	v_cmp_gt_u32_e32 vcc, s71, v16
	v_add_u32_e32 v16, -16, v2
	s_nop 0
	v_cndmask_b32_e32 v57, v197, v57, vcc
	v_cmp_gt_u32_e32 vcc, s71, v16
	v_subrev_u32_e32 v16, 17, v2
	s_nop 0
	v_cndmask_b32_e32 v58, v197, v58, vcc
	v_cmp_gt_u32_e32 vcc, s71, v16
	v_subrev_u32_e32 v16, 18, v2
	s_nop 0
	v_cndmask_b32_e32 v59, v197, v59, vcc
	v_cmp_gt_u32_e32 vcc, s71, v16
	v_subrev_u32_e32 v16, 19, v2
	s_nop 0
	v_cndmask_b32_e32 v60, v197, v60, vcc
	v_cmp_gt_u32_e32 vcc, s71, v16
	v_subrev_u32_e32 v16, 24, v2
	s_nop 0
	v_cndmask_b32_e32 v61, v197, v61, vcc
	v_cmp_gt_u32_e32 vcc, s71, v16
	v_subrev_u32_e32 v16, 25, v2
	s_nop 0
	v_cndmask_b32_e32 v62, v197, v62, vcc
	v_cmp_gt_u32_e32 vcc, s71, v16
	v_subrev_u32_e32 v16, 26, v2
	v_subrev_u32_e32 v2, 27, v2
	v_cndmask_b32_e32 v63, v197, v63, vcc
	v_cmp_gt_u32_e32 vcc, s71, v16
	s_nop 1
	v_cndmask_b32_e32 v64, v197, v64, vcc
	v_cmp_gt_u32_e32 vcc, s71, v2
	s_nop 1
	v_cndmask_b32_e32 v65, v197, v65, vcc
